# speedup vs baseline: 1.0258x; 1.0258x over previous
_Z13logits_kernelPKDv8_DF16bS1_PKfS3_PDv2_fS5_Pf:
	s_load_dwordx4 s[4:7], s[0:1], 0x0
	s_load_dwordx4 s[12:15], s[0:1], 0x10
	s_load_dwordx4 s[24:27], s[0:1], 0x20
	s_load_dwordx2 s[28:29], s[0:1], 0x30
	s_lshl_b32 s3, s2, 1
	s_and_b32 s3, s3, 14
	s_ashr_i32 s8, s2, 7
	s_bfe_u32 s10, s2, 0x40003
	s_add_i32 s3, s3, s8
	v_lshrrev_b32_e32 v1, 6, v0
	v_and_b32_e32 v2, 63, v0
	s_movk_i32 s11, 0x3000
	v_lshlrev_b32_e32 v2, 4, v2
	v_and_b32_e32 v5, 31, v0
	v_mad_u32_u24 v2, v1, s11, v2
	v_lshlrev_b32_e32 v5, 2, v5
	s_lshl_b32 s9, s3, 9
	v_add_u32_e32 v3, 0x1000, v2
	v_add_u32_e32 v4, 0x2000, v2
	v_add_u32_e32 v5, s9, v5
	s_mul_i32 s8, s10, 0xc000
	s_mul_i32 s9, s3, 0x30000
	s_waitcnt lgkmcnt(0)
	s_load_dword s22, s[14:15], 0x0
	global_load_dword v248, v5, s[12:13]
	global_load_dword v249, v5, s[12:13] offset:128
	global_load_dword v250, v5, s[12:13] offset:256
	global_load_dword v251, v5, s[12:13] offset:384
	s_add_u32 s4, s4, s8
	s_addc_u32 s5, s5, 0
	s_add_u32 s6, s6, s9
	s_addc_u32 s7, s7, 0
	s_add_u32 s16, s6, 0xc000
	s_addc_u32 s17, s7, 0
	s_add_u32 s18, s6, 0x18000
	s_addc_u32 s19, s7, 0
	s_add_u32 s20, s6, 0x24000
	s_addc_u32 s21, s7, 0
	global_load_dwordx4 v[8:11], v2, s[4:5]
	global_load_dwordx4 v[56:59], v2, s[6:7]
	global_load_dwordx4 v[104:107], v2, s[16:17]
	global_load_dwordx4 v[152:155], v2, s[18:19]
	global_load_dwordx4 v[200:203], v2, s[20:21]
	global_load_dwordx4 v[12:15], v2, s[4:5] offset:1024
	global_load_dwordx4 v[60:63], v2, s[6:7] offset:1024
	global_load_dwordx4 v[108:111], v2, s[16:17] offset:1024
	global_load_dwordx4 v[156:159], v2, s[18:19] offset:1024
	global_load_dwordx4 v[204:207], v2, s[20:21] offset:1024
	global_load_dwordx4 v[16:19], v2, s[4:5] offset:2048
	global_load_dwordx4 v[64:67], v2, s[6:7] offset:2048
	global_load_dwordx4 v[112:115], v2, s[16:17] offset:2048
	global_load_dwordx4 v[160:163], v2, s[18:19] offset:2048
	global_load_dwordx4 v[208:211], v2, s[20:21] offset:2048
	global_load_dwordx4 v[20:23], v2, s[4:5] offset:3072
	global_load_dwordx4 v[68:71], v2, s[6:7] offset:3072
	global_load_dwordx4 v[116:119], v2, s[16:17] offset:3072
	global_load_dwordx4 v[164:167], v2, s[18:19] offset:3072
	global_load_dwordx4 v[212:215], v2, s[20:21] offset:3072
	global_load_dwordx4 v[24:27], v3, s[4:5]
	global_load_dwordx4 v[72:75], v3, s[6:7]
	global_load_dwordx4 v[120:123], v3, s[16:17]
	global_load_dwordx4 v[168:171], v3, s[18:19]
	global_load_dwordx4 v[216:219], v3, s[20:21]
	global_load_dwordx4 v[28:31], v3, s[4:5] offset:1024
	global_load_dwordx4 v[76:79], v3, s[6:7] offset:1024
	global_load_dwordx4 v[124:127], v3, s[16:17] offset:1024
	global_load_dwordx4 v[172:175], v3, s[18:19] offset:1024
	global_load_dwordx4 v[220:223], v3, s[20:21] offset:1024
	global_load_dwordx4 v[32:35], v3, s[4:5] offset:2048
	global_load_dwordx4 v[80:83], v3, s[6:7] offset:2048
	global_load_dwordx4 v[128:131], v3, s[16:17] offset:2048
	global_load_dwordx4 v[176:179], v3, s[18:19] offset:2048
	global_load_dwordx4 v[224:227], v3, s[20:21] offset:2048
	global_load_dwordx4 v[36:39], v3, s[4:5] offset:3072
	global_load_dwordx4 v[84:87], v3, s[6:7] offset:3072
	global_load_dwordx4 v[132:135], v3, s[16:17] offset:3072
	global_load_dwordx4 v[180:183], v3, s[18:19] offset:3072
	global_load_dwordx4 v[228:231], v3, s[20:21] offset:3072
	global_load_dwordx4 v[40:43], v4, s[4:5]
	global_load_dwordx4 v[88:91], v4, s[6:7]
	global_load_dwordx4 v[136:139], v4, s[16:17]
	global_load_dwordx4 v[184:187], v4, s[18:19]
	global_load_dwordx4 v[232:235], v4, s[20:21]
	global_load_dwordx4 v[44:47], v4, s[4:5] offset:1024
	global_load_dwordx4 v[92:95], v4, s[6:7] offset:1024
	global_load_dwordx4 v[140:143], v4, s[16:17] offset:1024
	global_load_dwordx4 v[188:191], v4, s[18:19] offset:1024
	global_load_dwordx4 v[236:239], v4, s[20:21] offset:1024
	global_load_dwordx4 v[48:51], v4, s[4:5] offset:2048
	global_load_dwordx4 v[96:99], v4, s[6:7] offset:2048
	global_load_dwordx4 v[144:147], v4, s[16:17] offset:2048
	global_load_dwordx4 v[192:195], v4, s[18:19] offset:2048
	global_load_dwordx4 v[240:243], v4, s[20:21] offset:2048
	global_load_dwordx4 v[52:55], v4, s[4:5] offset:3072
	global_load_dwordx4 v[100:103], v4, s[6:7] offset:3072
	global_load_dwordx4 v[148:151], v4, s[16:17] offset:3072
	global_load_dwordx4 v[196:199], v4, s[18:19] offset:3072
	global_load_dwordx4 v[244:247], v4, s[20:21] offset:3072
	s_waitcnt vmcnt(58)
	v_mfma_f32_32x32x16_bf16 a[0:15], v[8:11], v[56:59], 0
	s_waitcnt vmcnt(57)
	v_mfma_f32_32x32x16_bf16 a[0:15], v[8:11], v[104:107], a[0:15]
	s_waitcnt vmcnt(56)
	v_mfma_f32_32x32x16_bf16 a[0:15], v[8:11], v[152:155], a[0:15]
	s_waitcnt vmcnt(55)
	v_mfma_f32_32x32x16_bf16 a[0:15], v[8:11], v[200:203], a[0:15]
	s_waitcnt vmcnt(53)
	v_mfma_f32_32x32x16_bf16 a[0:15], v[12:15], v[60:63], a[0:15]
	s_waitcnt vmcnt(52)
	v_mfma_f32_32x32x16_bf16 a[0:15], v[12:15], v[108:111], a[0:15]
	s_waitcnt vmcnt(51)
	v_mfma_f32_32x32x16_bf16 a[0:15], v[12:15], v[156:159], a[0:15]
	s_waitcnt vmcnt(50)
	v_mfma_f32_32x32x16_bf16 a[0:15], v[12:15], v[204:207], a[0:15]
	v_add_f32_e32 v8, 0, v248
	v_add_f32_e32 v8, v8, v249
	v_add_f32_e32 v8, v8, v250
	v_add_f32_e32 v8, v8, v251
	v_mov_b32_e32 v9, 0x3fb8aa3b
	s_waitcnt lgkmcnt(0)
	v_mul_f32_e32 v9, s22, v9
	v_exp_f32_e32 v9, v9
	v_add_f32_e32 v10, 0x2b8cbccc, v8
	v_div_scale_f32 v11, s[8:9], v10, v10, v9
	v_rcp_f32_e32 v12, v11
	v_div_scale_f32 v13, vcc, v9, v10, v9
	v_fma_f32 v14, -v11, v12, 1.0
	v_fmac_f32_e32 v12, v14, v12
	v_mul_f32_e32 v14, v13, v12
	v_fma_f32 v15, -v11, v14, v13
	v_fmac_f32_e32 v14, v15, v12
	v_fma_f32 v11, -v11, v14, v13
	v_div_fmas_f32 v11, v11, v12, v14
	v_div_fixup_f32 v9, v11, v10, v9
	v_lshlrev_b32_e32 v10, 2, v0
	v_add_u32_e32 v10, 0x4000, v10
	v_cmp_gt_u32_e32 vcc, 32, v0
	s_and_saveexec_b64 s[8:9], vcc
	ds_write2_b32 v10, v8, v9 offset0:128 offset1:160
	s_mov_b64 exec, s[8:9]
	s_waitcnt vmcnt(48)
	v_mfma_f32_32x32x16_bf16 a[0:15], v[16:19], v[64:67], a[0:15]
	s_waitcnt vmcnt(47)
	v_mfma_f32_32x32x16_bf16 a[0:15], v[16:19], v[112:115], a[0:15]
	s_waitcnt vmcnt(46)
	v_mfma_f32_32x32x16_bf16 a[0:15], v[16:19], v[160:163], a[0:15]
	s_waitcnt vmcnt(45)
	v_mfma_f32_32x32x16_bf16 a[0:15], v[16:19], v[208:211], a[0:15]
	s_waitcnt vmcnt(43)
	v_mfma_f32_32x32x16_bf16 a[0:15], v[20:23], v[68:71], a[0:15]
	s_waitcnt vmcnt(42)
	v_mfma_f32_32x32x16_bf16 a[0:15], v[20:23], v[116:119], a[0:15]
	s_waitcnt vmcnt(41)
	v_mfma_f32_32x32x16_bf16 a[0:15], v[20:23], v[164:167], a[0:15]
	s_waitcnt vmcnt(40)
	v_mfma_f32_32x32x16_bf16 a[0:15], v[20:23], v[212:215], a[0:15]
	s_waitcnt vmcnt(38)
	v_mfma_f32_32x32x16_bf16 a[0:15], v[24:27], v[72:75], a[0:15]
	s_waitcnt vmcnt(37)
	v_mfma_f32_32x32x16_bf16 a[0:15], v[24:27], v[120:123], a[0:15]
	s_waitcnt vmcnt(36)
	v_mfma_f32_32x32x16_bf16 a[0:15], v[24:27], v[168:171], a[0:15]
	s_waitcnt vmcnt(35)
	v_mfma_f32_32x32x16_bf16 a[0:15], v[24:27], v[216:219], a[0:15]
	s_waitcnt vmcnt(33)
	v_mfma_f32_32x32x16_bf16 a[0:15], v[28:31], v[76:79], a[0:15]
	s_waitcnt vmcnt(32)
	v_mfma_f32_32x32x16_bf16 a[0:15], v[28:31], v[124:127], a[0:15]
	s_waitcnt vmcnt(31)
	v_mfma_f32_32x32x16_bf16 a[0:15], v[28:31], v[172:175], a[0:15]
	s_waitcnt vmcnt(30)
	v_mfma_f32_32x32x16_bf16 a[0:15], v[28:31], v[220:223], a[0:15]
	s_waitcnt vmcnt(28)
	v_mfma_f32_32x32x16_bf16 a[0:15], v[32:35], v[80:83], a[0:15]
	s_waitcnt vmcnt(27)
	v_mfma_f32_32x32x16_bf16 a[0:15], v[32:35], v[128:131], a[0:15]
	s_waitcnt vmcnt(26)
	v_mfma_f32_32x32x16_bf16 a[0:15], v[32:35], v[176:179], a[0:15]
	s_waitcnt vmcnt(25)
	v_mfma_f32_32x32x16_bf16 a[0:15], v[32:35], v[224:227], a[0:15]
	s_waitcnt vmcnt(23)
	v_mfma_f32_32x32x16_bf16 a[0:15], v[36:39], v[84:87], a[0:15]
	s_waitcnt vmcnt(22)
	v_mfma_f32_32x32x16_bf16 a[0:15], v[36:39], v[132:135], a[0:15]
	s_waitcnt vmcnt(21)
	v_mfma_f32_32x32x16_bf16 a[0:15], v[36:39], v[180:183], a[0:15]
	s_waitcnt vmcnt(20)
	v_mfma_f32_32x32x16_bf16 a[0:15], v[36:39], v[228:231], a[0:15]
	s_waitcnt vmcnt(18)
	v_mfma_f32_32x32x16_bf16 a[0:15], v[40:43], v[88:91], a[0:15]
	s_waitcnt vmcnt(17)
	v_mfma_f32_32x32x16_bf16 a[0:15], v[40:43], v[136:139], a[0:15]
	s_waitcnt vmcnt(16)
	v_mfma_f32_32x32x16_bf16 a[0:15], v[40:43], v[184:187], a[0:15]
	s_waitcnt vmcnt(15)
	v_mfma_f32_32x32x16_bf16 a[0:15], v[40:43], v[232:235], a[0:15]
	s_waitcnt vmcnt(13)
	v_mfma_f32_32x32x16_bf16 a[0:15], v[44:47], v[92:95], a[0:15]
	s_waitcnt vmcnt(12)
	v_mfma_f32_32x32x16_bf16 a[0:15], v[44:47], v[140:143], a[0:15]
	s_waitcnt vmcnt(11)
	v_mfma_f32_32x32x16_bf16 a[0:15], v[44:47], v[188:191], a[0:15]
	s_waitcnt vmcnt(10)
	v_mfma_f32_32x32x16_bf16 a[0:15], v[44:47], v[236:239], a[0:15]
	s_waitcnt vmcnt(8)
	v_mfma_f32_32x32x16_bf16 a[0:15], v[48:51], v[96:99], a[0:15]
	s_waitcnt vmcnt(7)
	v_mfma_f32_32x32x16_bf16 a[0:15], v[48:51], v[144:147], a[0:15]
	s_waitcnt vmcnt(6)
	v_mfma_f32_32x32x16_bf16 a[0:15], v[48:51], v[192:195], a[0:15]
	s_waitcnt vmcnt(5)
	v_mfma_f32_32x32x16_bf16 a[0:15], v[48:51], v[240:243], a[0:15]
	v_mul_u32_u24_e32 v1, 0x1080, v1
	s_movk_i32 s4, 0x7f
	s_movk_i32 s6, 0x84
	v_cmp_lt_u32_e32 vcc, s4, v0
	v_lshrrev_b32_e32 v11, 3, v0
	v_and_b32_e32 v10, 31, v0
	v_and_b32_e32 v11, 4, v11
	v_mul_u32_u24_e32 v11, 0x84, v11
	v_lshlrev_b32_e32 v9, 2, v10
	v_bfe_u32 v6, v0, 2, 5
	v_and_b32_e32 v7, 3, v0
	v_add3_u32 v1, v1, v11, v9
	v_lshlrev_b32_e32 v8, 3, v7
	s_waitcnt vmcnt(3)
	v_mfma_f32_32x32x16_bf16 a[0:15], v[52:55], v[100:103], a[0:15]
	s_waitcnt vmcnt(2)
	v_mfma_f32_32x32x16_bf16 a[0:15], v[52:55], v[148:151], a[0:15]
	s_waitcnt vmcnt(1)
	v_mfma_f32_32x32x16_bf16 a[0:15], v[52:55], v[196:199], a[0:15]
	s_waitcnt vmcnt(0)
	v_mfma_f32_32x32x16_bf16 a[0:15], v[52:55], v[244:247], a[0:15]
	s_nop 11
	ds_write_b32 v1, a0
	ds_write_b32 v1, a1 offset:132
	ds_write_b32 v1, a2 offset:264
	ds_write_b32 v1, a3 offset:396
	ds_write_b32 v1, a4 offset:1056
	ds_write_b32 v1, a5 offset:1188
	ds_write_b32 v1, a6 offset:1320
	ds_write_b32 v1, a7 offset:1452
	ds_write_b32 v1, a8 offset:2112
	ds_write_b32 v1, a9 offset:2244
	ds_write_b32 v1, a10 offset:2376
	ds_write_b32 v1, a11 offset:2508
	ds_write_b32 v1, a12 offset:3168
	ds_write_b32 v1, a13 offset:3300
	ds_write_b32 v1, a14 offset:3432
	ds_write_b32 v1, a15 offset:3564
	v_bfe_u32 v6, v0, 2, 5
	v_and_b32_e32 v7, 3, v0
	v_lshlrev_b32_e32 v9, 3, v7
	v_readfirstlane_b32 s30, v0
	v_sub_u32_e32 v10, v6, v9
	s_waitcnt lgkmcnt(0)
	s_barrier
	s_cmpk_ge_u32 s30, 0x80
	s_cbranch_scc1 .Llg_k1
	v_mul_u32_u24_e32 v2, 0x84, v6
	v_lshlrev_b32_e32 v8, 5, v7
	v_add_u32_e32 v2, v2, v8
	v_add_u32_e32 v8, 0x4280, v8
	v_add_u32_e32 v3, 0x1080, v2
	v_add_u32_e32 v4, 0x2100, v2
	v_add_u32_e32 v5, 0x3180, v2
	ds_read_b128 v[48:51], v8
	ds_read_b128 v[52:55], v8 offset:16
	ds_read2_b32 v[16:17], v2 offset0:0 offset1:1
	ds_read2_b32 v[18:19], v2 offset0:2 offset1:3
	ds_read2_b32 v[20:21], v2 offset0:4 offset1:5
	ds_read2_b32 v[22:23], v2 offset0:6 offset1:7
	ds_read2_b32 v[24:25], v3 offset0:0 offset1:1
	ds_read2_b32 v[26:27], v3 offset0:2 offset1:3
	ds_read2_b32 v[28:29], v3 offset0:4 offset1:5
	ds_read2_b32 v[30:31], v3 offset0:6 offset1:7
	ds_read2_b32 v[32:33], v4 offset0:0 offset1:1
	ds_read2_b32 v[34:35], v4 offset0:2 offset1:3
	ds_read2_b32 v[36:37], v4 offset0:4 offset1:5
	ds_read2_b32 v[38:39], v4 offset0:6 offset1:7
	s_waitcnt lgkmcnt(4)
	ds_read2_b32 v[40:41], v5 offset0:0 offset1:1
	ds_read2_b32 v[42:43], v5 offset0:2 offset1:3
	ds_read2_b32 v[44:45], v5 offset0:4 offset1:5
	ds_read2_b32 v[46:47], v5 offset0:6 offset1:7
	s_waitcnt lgkmcnt(0)
	s_branch .Llg_join
.Llg_k1:
	v_mul_u32_u24_e32 v2, 0x420, v7
	v_lshlrev_b32_e32 v8, 2, v6
	v_add_u32_e32 v2, v2, v8
	v_add_u32_e32 v3, 0x1080, v2
	v_add_u32_e32 v4, 0x2100, v2
	v_add_u32_e32 v5, 0x3180, v2
	ds_read_b32 v48, v8 offset:17024
	ds_read2_b32 v[16:17], v2 offset0:0 offset1:33
	ds_read2_b32 v[18:19], v2 offset0:66 offset1:99
	ds_read2_b32 v[20:21], v2 offset0:132 offset1:165
	ds_read2_b32 v[22:23], v2 offset0:198 offset1:231
	ds_read2_b32 v[24:25], v3 offset0:0 offset1:33
	ds_read2_b32 v[26:27], v3 offset0:66 offset1:99
	ds_read2_b32 v[28:29], v3 offset0:132 offset1:165
	ds_read2_b32 v[30:31], v3 offset0:198 offset1:231
	ds_read2_b32 v[32:33], v4 offset0:0 offset1:33
	ds_read2_b32 v[34:35], v4 offset0:66 offset1:99
	ds_read2_b32 v[36:37], v4 offset0:132 offset1:165
	ds_read2_b32 v[38:39], v4 offset0:198 offset1:231
	s_waitcnt lgkmcnt(4)
	ds_read2_b32 v[40:41], v5 offset0:0 offset1:33
	ds_read2_b32 v[42:43], v5 offset0:66 offset1:99
	ds_read2_b32 v[44:45], v5 offset0:132 offset1:165
	ds_read2_b32 v[46:47], v5 offset0:198 offset1:231
	s_waitcnt lgkmcnt(0)
	v_mov_b32_e32 v49, v48
	v_mov_b32_e32 v50, v48
	v_mov_b32_e32 v51, v48
	v_mov_b32_e32 v52, v48
	v_mov_b32_e32 v53, v48
	v_mov_b32_e32 v54, v48
	v_mov_b32_e32 v55, v48
.Llg_join:
	v_add_f32_e32 v16, v16, v24
	v_add_f32_e32 v32, v32, v40
	v_add_f32_e32 v17, v17, v25
	v_add_f32_e32 v33, v33, v41
	v_add_f32_e32 v18, v18, v26
	v_add_f32_e32 v34, v34, v42
	v_add_f32_e32 v19, v19, v27
	v_add_f32_e32 v35, v35, v43
	v_add_f32_e32 v20, v20, v28
	v_add_f32_e32 v36, v36, v44
	v_add_f32_e32 v21, v21, v29
	v_add_f32_e32 v37, v37, v45
	v_add_f32_e32 v22, v22, v30
	v_add_f32_e32 v38, v38, v46
	v_add_f32_e32 v23, v23, v31
	v_add_f32_e32 v39, v39, v47
	v_add_f32_e32 v16, v16, v32
	v_add_f32_e32 v17, v17, v33
	v_add_f32_e32 v18, v18, v34
	v_add_f32_e32 v19, v19, v35
	v_add_f32_e32 v20, v20, v36
	v_add_f32_e32 v21, v21, v37
	v_add_f32_e32 v22, v22, v38
	v_add_f32_e32 v23, v23, v39
	v_mul_f32_e32 v16, v16, v48
	v_mul_f32_e32 v17, v17, v49
	v_mul_f32_e32 v18, v18, v50
	v_mul_f32_e32 v19, v19, v51
	v_mul_f32_e32 v20, v20, v52
	v_mul_f32_e32 v21, v21, v53
	v_mul_f32_e32 v22, v22, v54
	v_mul_f32_e32 v23, v23, v55
	v_max3_f32 v56, v16, v17, v18
	v_max3_f32 v57, v19, v20, v21
	v_max3_f32 v56, v56, v22, v23
	v_max_f32_e32 v56, v56, v57
	v_mov_b32_e32 v58, 0xff800000
	v_cmp_eq_u32_e32 vcc, 0, v10
	s_nop 1
	v_cndmask_b32_e32 v58, v58, v16, vcc
	v_cmp_eq_u32_e32 vcc, 1, v10
	s_nop 1
	v_cndmask_b32_e32 v58, v58, v17, vcc
	v_cmp_eq_u32_e32 vcc, 2, v10
	s_nop 1
	v_cndmask_b32_e32 v58, v58, v18, vcc
	v_cmp_eq_u32_e32 vcc, 3, v10
	s_nop 1
	v_cndmask_b32_e32 v58, v58, v19, vcc
	v_cmp_eq_u32_e32 vcc, 4, v10
	s_nop 1
	v_cndmask_b32_e32 v58, v58, v20, vcc
	v_cmp_eq_u32_e32 vcc, 5, v10
	s_nop 1
	v_cndmask_b32_e32 v58, v58, v21, vcc
	v_cmp_eq_u32_e32 vcc, 6, v10
	s_nop 1
	v_cndmask_b32_e32 v58, v58, v22, vcc
	v_cmp_eq_u32_e32 vcc, 7, v10
	s_nop 1
	v_cndmask_b32_e32 v58, v58, v23, vcc
	s_nop 1
	v_max_f32_dpp v57, v56, v56 quad_perm:[1,0,3,2] row_mask:0xf bank_mask:0xf
	s_nop 1
	v_max_f32_dpp v56, v57, v57 quad_perm:[2,3,0,1] row_mask:0xf bank_mask:0xf
	s_nop 0
	v_sub_f32_e32 v24, v16, v56
	v_sub_f32_e32 v25, v17, v56
	v_sub_f32_e32 v26, v18, v56
	v_sub_f32_e32 v27, v19, v56
	v_sub_f32_e32 v28, v20, v56
	v_sub_f32_e32 v29, v21, v56
	v_sub_f32_e32 v30, v22, v56
	v_sub_f32_e32 v31, v23, v56
	v_mul_f32_e32 v24, 0x3fb8aa3b, v24
	v_mul_f32_e32 v25, 0x3fb8aa3b, v25
	v_mul_f32_e32 v26, 0x3fb8aa3b, v26
	v_mul_f32_e32 v27, 0x3fb8aa3b, v27
	v_mul_f32_e32 v28, 0x3fb8aa3b, v28
	v_mul_f32_e32 v29, 0x3fb8aa3b, v29
	v_mul_f32_e32 v30, 0x3fb8aa3b, v30
	v_mul_f32_e32 v31, 0x3fb8aa3b, v31
	v_exp_f32_e32 v24, v24
	v_exp_f32_e32 v25, v25
	v_exp_f32_e32 v26, v26
	v_exp_f32_e32 v27, v27
	v_exp_f32_e32 v28, v28
	v_exp_f32_e32 v29, v29
	v_exp_f32_e32 v30, v30
	v_exp_f32_e32 v31, v31
	s_nop 0
	v_add_f32_e32 v24, v24, v25
	v_add_f32_e32 v26, v26, v27
	v_add_f32_e32 v28, v28, v29
	v_add_f32_e32 v30, v30, v31
	v_add_f32_e32 v24, v24, v26
	v_add_f32_e32 v28, v28, v30
	v_add_f32_e32 v59, v24, v28
	s_nop 1
	v_add_f32_dpp v60, v59, v59 quad_perm:[1,0,3,2] row_mask:0xf bank_mask:0xf
	v_max_f32_dpp v61, v58, v58 quad_perm:[1,0,3,2] row_mask:0xf bank_mask:0xf
	s_nop 1
	v_add_f32_dpp v57, v60, v60 quad_perm:[2,3,0,1] row_mask:0xf bank_mask:0xf
	v_max_f32_dpp v58, v61, v61 quad_perm:[2,3,0,1] row_mask:0xf bank_mask:0xf
	v_cmp_eq_u32_e32 vcc, 0, v7
	s_and_saveexec_b64 s[4:5], vcc
	s_cbranch_execz .Llg_end
	s_cmpk_ge_u32 s30, 0x80
	s_cbranch_scc1 .Llg_st1
	s_lshr_b32 s8, s3, 1
	s_lshl_b32 s8, s8, 9
	s_lshl_b32 s9, s10, 5
	s_add_i32 s8, s8, s9
	s_and_b32 s11, s3, 1
	s_lshl_b32 s11, s11, 3
	v_add_u32_e32 v2, s8, v6
	v_lshlrev_b32_e32 v2, 4, v2
	v_add_u32_e32 v2, s11, v2
	global_store_dwordx2 v2, v[56:57], s[24:25]
	s_cmp_lg_u32 s10, s3
	s_cbranch_scc1 .Llg_end
	v_add_u32_e32 v3, s9, v6
	v_lshlrev_b32_e32 v3, 2, v3
	global_store_dword v3, v58, s[28:29]
	s_branch .Llg_end
.Llg_st1:
	s_lshr_b32 s8, s10, 1
	s_lshl_b32 s8, s8, 9
	s_lshl_b32 s9, s3, 5
	s_add_i32 s8, s8, s9
	s_and_b32 s11, s10, 1
	s_lshl_b32 s11, s11, 3
	v_add_u32_e32 v2, s8, v6
	v_lshlrev_b32_e32 v2, 4, v2
	v_add_u32_e32 v2, s11, v2
	global_store_dwordx2 v2, v[56:57], s[26:27]
	s_cmp_lg_u32 s10, 0
	s_cbranch_scc1 .Llg_end
	v_lshlrev_b32_e32 v4, 2, v6
	ds_read_b32 v5, v4 offset:16896
	v_add_u32_e32 v3, s9, v6
	v_lshlrev_b32_e32 v3, 2, v3
	s_waitcnt lgkmcnt(0)
	global_store_dword v3, v5, s[28:29] offset:2048

	.amdhsa_kernel _Z13logits_kernelPKDv8_DF16bS1_PKfS3_PDv2_fS5_Pf
		.amdhsa_group_segment_fixed_size 17152
		.amdhsa_private_segment_fixed_size 0
		.amdhsa_kernarg_size 56
		.amdhsa_user_sgpr_count 2
		.amdhsa_user_sgpr_dispatch_ptr 0
		.amdhsa_user_sgpr_queue_ptr 0
		.amdhsa_user_sgpr_kernarg_segment_ptr 1
		.amdhsa_user_sgpr_dispatch_id 0
		.amdhsa_user_sgpr_kernarg_preload_length 0
		.amdhsa_user_sgpr_kernarg_preload_offset 0
		.amdhsa_user_sgpr_private_segment_size 0
		.amdhsa_uses_dynamic_stack 0
		.amdhsa_enable_private_segment 0
		.amdhsa_system_sgpr_workgroup_id_x 1
		.amdhsa_system_sgpr_workgroup_id_y 0
		.amdhsa_system_sgpr_workgroup_id_z 0
		.amdhsa_system_sgpr_workgroup_info 0
		.amdhsa_system_vgpr_workitem_id 0
		.amdhsa_next_free_vgpr 268
		.amdhsa_next_free_sgpr 31
		.amdhsa_accum_offset 252
		.amdhsa_reserve_vcc 1
		.amdhsa_float_round_mode_32 0
		.amdhsa_float_round_mode_16_64 0
		.amdhsa_float_denorm_mode_32 3
		.amdhsa_float_denorm_mode_16_64 3
		.amdhsa_dx10_clamp 1
		.amdhsa_ieee_mode 1
		.amdhsa_fp16_overflow 0
		.amdhsa_tg_split 0
		.amdhsa_exception_fp_ieee_invalid_op 0
		.amdhsa_exception_fp_denorm_src 0
		.amdhsa_exception_fp_ieee_div_zero 0
		.amdhsa_exception_fp_ieee_overflow 0
		.amdhsa_exception_fp_ieee_underflow 0
		.amdhsa_exception_fp_ieee_inexact 0
		.amdhsa_exception_int_div_zero 0
	.end_amdhsa_kernel

amdhsa.kernels:
  - .agpr_count:     0
    .args:
      - .actual_access:  read_only
        .address_space:  global
        .offset:         0
        .size:           8
        .value_kind:     global_buffer
      - .actual_access:  read_only
        .address_space:  global
        .offset:         8
        .size:           8
        .value_kind:     global_buffer
      - .actual_access:  read_only
        .address_space:  global
        .offset:         16
        .size:           8
        .value_kind:     global_buffer
      - .actual_access:  write_only
        .address_space:  global
        .offset:         24
        .size:           8
        .value_kind:     global_buffer
      - .actual_access:  write_only
        .address_space:  global
        .offset:         32
        .size:           8
        .value_kind:     global_buffer
      - .actual_access:  write_only
        .address_space:  global
        .offset:         40
        .size:           8
        .value_kind:     global_buffer
    .group_segment_fixed_size: 100880
    .kernarg_segment_align: 8
    .kernarg_segment_size: 48
    .language:       OpenCL C
    .language_version:
      - 2
      - 0
    .max_flat_workgroup_size: 768
    .name:           _Z14seg_sum_kernelPKfS0_S0_PDv8_DF16bS2_Pf
    .private_segment_fixed_size: 0
    .sgpr_count:     42
    .sgpr_spill_count: 0
    .symbol:         _Z14seg_sum_kernelPKfS0_S0_PDv8_DF16bS2_Pf.kd
    .uniform_work_group_size: 1
    .uses_dynamic_stack: false
    .vgpr_count:     142
    .vgpr_spill_count: 0
    .wavefront_size: 64
  - .agpr_count:     16
    .args:
      - .actual_access:  read_only
        .address_space:  global
        .offset:         0
        .size:           8
        .value_kind:     global_buffer
      - .actual_access:  read_only
        .address_space:  global
        .offset:         8
        .size:           8
        .value_kind:     global_buffer
      - .actual_access:  read_only
        .address_space:  global
        .offset:         16
        .size:           8
        .value_kind:     global_buffer
      - .actual_access:  read_only
        .address_space:  global
        .offset:         24
        .size:           8
        .value_kind:     global_buffer
      - .actual_access:  write_only
        .address_space:  global
        .offset:         32
        .size:           8
        .value_kind:     global_buffer
      - .actual_access:  write_only
        .address_space:  global
        .offset:         40
        .size:           8
        .value_kind:     global_buffer
      - .actual_access:  write_only
        .address_space:  global
        .offset:         48
        .size:           8
        .value_kind:     global_buffer
    .group_segment_fixed_size: 17152
    .kernarg_segment_align: 8
    .kernarg_segment_size: 56
    .language:       OpenCL C
    .language_version:
      - 2
      - 0
    .max_flat_workgroup_size: 256
    .name:           _Z13logits_kernelPKDv8_DF16bS1_PKfS3_PDv2_fS5_Pf
    .private_segment_fixed_size: 0
    .sgpr_count:     37
    .sgpr_spill_count: 0
    .symbol:         _Z13logits_kernelPKDv8_DF16bS1_PKfS3_PDv2_fS5_Pf.kd
    .uniform_work_group_size: 1
    .uses_dynamic_stack: false
    .vgpr_count:     268
    .vgpr_spill_count: 0
    .wavefront_size: 64
  - .agpr_count:     0
    .args:
      - .actual_access:  read_only
        .address_space:  global
        .offset:         0
        .size:           8
        .value_kind:     global_buffer
      - .actual_access:  read_only
        .address_space:  global
        .offset:         8
        .size:           8
        .value_kind:     global_buffer
      - .actual_access:  read_only
        .address_space:  global
        .offset:         16
        .size:           8
        .value_kind:     global_buffer
      - .actual_access:  read_only
        .address_space:  global
        .offset:         24
        .size:           8
        .value_kind:     global_buffer
      - .actual_access:  write_only
        .address_space:  global
        .offset:         32
        .size:           8
        .value_kind:     global_buffer
    .group_segment_fixed_size: 128
    .kernarg_segment_align: 8
    .kernarg_segment_size: 40
    .language:       OpenCL C
    .language_version:
      - 2
      - 0
    .max_flat_workgroup_size: 1024
    .name:           _Z12final_kernelPKDv4_fS1_PKfS3_Pf
    .private_segment_fixed_size: 0
    .sgpr_count:     15
    .sgpr_spill_count: 0
    .symbol:         _Z12final_kernelPKDv4_fS1_PKfS3_Pf.kd
    .uniform_work_group_size: 1
    .uses_dynamic_stack: false
    .vgpr_count:     50
    .vgpr_spill_count: 0
    .wavefront_size: 64
